# diff softmax: row-max chain only on first tile or sum trigger; in-place exp, scores recomputed by MFMA on the rare path; on top of v034
# speedup vs baseline: 1.0041x; 1.0041x over previous
; __device__ __forceinline__ int crow(int r, int hi) { return (r & 3) + 8 * (r >> 2) + 4 * hi; }
; __device__ __forceinline__ void smax_tile(f32x16& p0, f32x16& p1, float& mhat, float& l_reg, f32x16 (&o)[4], float* al_l, const bool first, int r32, int hi,
;                                           bf16x8& pa0, bf16x8& pa1, bf16x8& pa2, bf16x8& pa3) {
;     ...
;     if (__builtin_expect(first || __any(rm > THRL), 0)) {
;         const float dl = first ? rm : fmaxf(rm, 0.f);
;         mhat += dl;
; #pragma unroll
;         for (int r = 0; r < 16; ++r) { p0[r] -= dl; p1[r] -= dl; }
;         if (!first) { const float f = __builtin_amdgcn_exp2f(-dl); l_reg *= f;
;             if (hi == 0) al_l[r32] = f; asm volatile("s_waitcnt lgkmcnt(0)" ::: "memory");
; #pragma unroll
;             for (int d = 0; d < 4; ++d)
; #pragma unroll
;                 for (int r = 0; r < 16; ++r) o[d][r] *= al_l[crow(r, hi)]; }
;     }
; #pragma unroll
;     for (int r = 0; r < 16; ++r) p0[r] = __builtin_amdgcn_exp2f(p0[r]);
; #pragma unroll
;     for (int r = 0; r < 16; ++r) p1[r] = __builtin_amdgcn_exp2f(p1[r]);
;     float ps = p0[0];
; #pragma unroll
;     for (int r = 1; r < 16; ++r) ps += p0[r];
; #pragma unroll
;     for (int r = 0; r < 16; ++r) ps += p1[r];
;     { auto rr = __builtin_amdgcn_permlane32_swap(__float_as_uint(ps), __float_as_uint(ps), false, false); ps = __uint_as_float(rr[0]) + __uint_as_float(rr[1]); }
;     l_reg += ps;
.LBB0_650:
	s_cmp_eq_u32 s44, s44
	v_add_f32_e32 v158, v158, v128
	v_sub_f32_e32 v111, v111, v128
	v_sub_f32_e32 v110, v110, v128
	v_sub_f32_e32 v109, v109, v128
	v_sub_f32_e32 v108, v108, v128
	v_sub_f32_e32 v107, v107, v128
	v_sub_f32_e32 v106, v106, v128
	v_sub_f32_e32 v105, v105, v128
	v_sub_f32_e32 v104, v104, v128
	v_sub_f32_e32 v103, v103, v128
	v_sub_f32_e32 v102, v102, v128
	v_sub_f32_e32 v101, v101, v128
	v_sub_f32_e32 v100, v100, v128
	v_sub_f32_e32 v99, v99, v128
	v_sub_f32_e32 v98, v98, v128
	v_sub_f32_e32 v97, v97, v128
	v_sub_f32_e32 v96, v96, v128
	v_sub_f32_e32 v95, v95, v128
	v_sub_f32_e32 v94, v94, v128
	v_sub_f32_e32 v93, v93, v128
	v_sub_f32_e32 v92, v92, v128
	v_sub_f32_e32 v91, v91, v128
	v_sub_f32_e32 v90, v90, v128
	v_sub_f32_e32 v89, v89, v128
	v_sub_f32_e32 v88, v88, v128
	v_sub_f32_e32 v87, v87, v128
	v_sub_f32_e32 v86, v86, v128
	v_sub_f32_e32 v85, v85, v128
	v_sub_f32_e32 v84, v84, v128
	v_sub_f32_e32 v83, v83, v128
	v_sub_f32_e32 v82, v82, v128
	v_sub_f32_e32 v81, v81, v128
	v_sub_f32_e32 v80, v80, v128
.LBB0_651:
	v_exp_f32_e32 v96, v96
	v_exp_f32_e32 v97, v97
	v_exp_f32_e32 v98, v98
	v_exp_f32_e32 v99, v99
	v_exp_f32_e32 v100, v100
	v_exp_f32_e32 v101, v101
	v_add_f32_e32 v128, v96, v97
	v_exp_f32_e32 v102, v102
	v_add_f32_e32 v128, v98, v128
	v_exp_f32_e32 v103, v103
	v_add_f32_e32 v128, v99, v128
	v_exp_f32_e32 v104, v104
	v_add_f32_e32 v128, v100, v128
	v_exp_f32_e32 v105, v105
	v_add_f32_e32 v128, v101, v128
	v_exp_f32_e32 v106, v106
	v_add_f32_e32 v128, v102, v128
	v_exp_f32_e32 v107, v107
	v_add_f32_e32 v128, v103, v128
	v_exp_f32_e32 v108, v108
	v_add_f32_e32 v128, v104, v128
	v_exp_f32_e32 v109, v109
	v_add_f32_e32 v128, v105, v128
	v_exp_f32_e32 v110, v110
	v_add_f32_e32 v128, v106, v128
	v_exp_f32_e32 v111, v111
	v_add_f32_e32 v128, v107, v128
	v_exp_f32_e32 v80, v80
	v_add_f32_e32 v128, v108, v128
	v_exp_f32_e32 v81, v81
	v_add_f32_e32 v128, v109, v128
	v_exp_f32_e32 v82, v82
	v_add_f32_e32 v128, v110, v128
	v_exp_f32_e32 v83, v83
	v_add_f32_e32 v128, v111, v128
	v_exp_f32_e32 v84, v84
	v_add_f32_e32 v128, v80, v128
	v_exp_f32_e32 v85, v85
	v_add_f32_e32 v128, v81, v128
	v_exp_f32_e32 v86, v86
	v_add_f32_e32 v128, v82, v128
	v_exp_f32_e32 v87, v87
	v_add_f32_e32 v128, v83, v128
	v_exp_f32_e32 v88, v88
	v_add_f32_e32 v128, v84, v128
	v_exp_f32_e32 v89, v89
	v_add_f32_e32 v128, v85, v128
	v_exp_f32_e32 v90, v90
	v_add_f32_e32 v128, v86, v128
	v_exp_f32_e32 v91, v91
	v_add_f32_e32 v128, v87, v128
	v_exp_f32_e32 v92, v92
	v_add_f32_e32 v128, v88, v128
	v_exp_f32_e32 v93, v93
	v_add_f32_e32 v128, v89, v128
	v_exp_f32_e32 v94, v94
	v_add_f32_e32 v128, v90, v128
	v_exp_f32_e32 v95, v95
	v_add_f32_e32 v128, v91, v128
	v_add_f32_e32 v128, v92, v128
	v_add_f32_e32 v128, v93, v128
	v_add_f32_e32 v128, v94, v128
	v_add_f32_e32 v128, v95, v128
	v_mov_b32_e32 v129, v128
	v_cvt_pk_bf16_f32 v162, v96, v97
	v_cvt_pk_bf16_f32 v163, v98, v99
	v_permlane32_swap_b32_e32 v128, v129
	v_add_f32_e32 v128, v128, v129
	s_cbranch_scc1 .Lmy_d_tail
	v_cmp_lt_f32_e32 vcc, 0x43000000, v128
	s_cbranch_vccnz .Lmy_d_recomp
; #define SBAR() __builtin_amdgcn_sched_barrier(0)
; __device__ __forceinline__ void smax_tile(f32x16& p0, f32x16& p1, float& mhat, float& l_reg, f32x16 (&o)[4], float* al_l, const bool first, int r32, int hi,
;                                           bf16x8& pa0, bf16x8& pa1, bf16x8& pa2, bf16x8& pa3) {
;     ...
;     l_reg += ps;
;     ...
;     PK4(p0, 0, pa0); PK4(p0, 8, pa1); PK4(p1, 0, pa2); PK4(p1, 8, pa3);
; template <int DQK, bool HASQK, bool HASPV, int J>
; __device__ __forceinline__ void slot_read(bf16x8 (&kf)[DQK / 16][2], s16x4 (&vf)[4][8], const int (&ka_)[4], int vb_) {
;     constexpr int NQS = HASQK ? 2 * (DQK / 16) : 0, NS = NQS + (HASPV ? 16 : 0);
;     if constexpr (J < NQS) { constexpr int d0 = J >> 1, h = J & 1; dsr128<(d0 >> 2) * 128 + h * 32 * DQK * 2>(kf[d0][h], ka_[d0 & 3]); }
;     else if constexpr (J < NS) { constexpr int q = J - NQS, g = q >> 2, d = q & 3; dstr64<v_rd_off(d, g, 0)>(vf[g][2 * d], vb_); dstr64<v_rd_off(d, g, 1)>(vf[g][2 * d + 1], vb_); }
; }
; template <int DQK, bool HASQK, bool HASPV, int J> ...
;     constexpr int NQS = HASQK ? 2 * (DQK / 16) : 0, NS = NQS + (HASPV ? 16 : 0);
;     if constexpr (J < NS) {
;         constexpr int rd1 = (J + 1 < NS) ? ((J + 1 < NQS) ? 1 : 2) : 0, rd2 = (J + 2 < NS) ? ((J + 2 < NQS) ? 1 : 2) : 0, rd3 = (J + 3 < NS) ? ((J + 3 < NQS) ? 1 : 2) : 0, NW = rd1 + rd2 + rd3;
;     ...
;         if constexpr (J < NQS) { constexpr int d0 = J >> 1, h = J & 1;
;             LWN1(kf[d0][h]); SBAR();
;             if constexpr (h == 0) p0 = __builtin_amdgcn_mfma_f32_32x32x16_bf16(kf[d0][0], qr[d0], (d0 == 0) ? negm : p0, 0, 0, 0);
;             else p1 = __builtin_amdgcn_mfma_f32_32x32x16_bf16(kf[d0][1], qr[d0], (d0 == 0) ? negm : p1, 0, 0, 0);
;         } else { constexpr int q = J - NQS, g = q >> 2, d = q & 3;
;             LWN2(vf[g][2 * d], vf[g][2 * d + 1]); SBAR();
;             o[d] = __builtin_amdgcn_mfma_f32_32x32x16_bf16(pa[g], (bf16x8){vf[g][2 * d][0], vf[g][2 * d][1], vf[g][2 * d][2], vf[g][2 * d][3], vf[g][2 * d + 1][0], vf[g][2 * d + 1][1], vf[g][2 * d + 1][2], vf[g][2 * d + 1][3]}, o[d], 0, 0, 0);
;         }
;     ...
;         SBAR();
;         slot_read<DQK, HASQK, HASPV, J + 4>(kf, vf, ka_, vb_);
;         SBAR();
;         slot_run<DQK, HASQK, HASPV, J + 1>(kf, vf, ka_, vb_, qr, p0, p1, negm, o, pa);
;     }
; }
.Lmy_d_tail:
	v_add_f32_e32 v159, v159, v128
	v_cvt_pk_bf16_f32 v164, v100, v101
	v_cvt_pk_bf16_f32 v165, v102, v103
	v_cvt_pk_bf16_f32 v166, v104, v105
	v_cvt_pk_bf16_f32 v167, v106, v107
	v_cvt_pk_bf16_f32 v168, v108, v109
	v_cvt_pk_bf16_f32 v169, v110, v111
	v_cvt_pk_bf16_f32 v132, v80, v81
	v_cvt_pk_bf16_f32 v133, v82, v83
	v_cvt_pk_bf16_f32 v134, v84, v85
	v_cvt_pk_bf16_f32 v135, v86, v87
	v_cvt_pk_bf16_f32 v128, v88, v89
	v_cvt_pk_bf16_f32 v129, v90, v91
	v_cvt_pk_bf16_f32 v130, v92, v93
	v_cvt_pk_bf16_f32 v131, v94, v95
	s_cmp_lg_u32 s86, 0
	s_waitcnt lgkmcnt(0)
	s_barrier
	s_cselect_b32 s46, s87, 0x8000
	s_lshl_b32 s47, s86, 13
	v_add_u32_e32 v81, s47, v141
	v_add_u32_e32 v82, s47, v143
	ds_read_b128 v[170:173], v81 offset:0
	ds_read_b128 v[174:177], v81 offset:0x1000
	ds_read_b128 v[178:181], v82 offset:0
	ds_read_b128 v[182:185], v82 offset:0x1000
	v_xor_b32_e32 v80, 0x80000000, v158
	v_add_u32_e32 v186, s47, v160
	v_add_u32_e32 v187, s47, v161
	v_add_u32_e32 v188, s46, v157
	v_mov_b32_e32 v81, v80
	v_mov_b32_e32 v82, v80
	v_mov_b32_e32 v83, v80
	v_mov_b32_e32 v84, v80
	v_mov_b32_e32 v85, v80
	v_mov_b32_e32 v86, v80
	v_mov_b32_e32 v87, v80
	v_mov_b32_e32 v88, v80
	v_mov_b32_e32 v89, v80
	v_mov_b32_e32 v90, v80
	v_mov_b32_e32 v91, v80
	v_mov_b32_e32 v92, v80
	v_mov_b32_e32 v93, v80
	v_mov_b32_e32 v94, v80
	v_mov_b32_e32 v95, v80
	s_waitcnt lgkmcnt(3)
	s_nop 1
	v_mfma_f32_32x32x16_bf16 v[96:111], v[170:173], v[112:115], v[80:95]
	ds_read_b128 v[170:173], v186 offset:0
	s_waitcnt lgkmcnt(3)
	s_nop 0
	v_mfma_f32_32x32x16_bf16 v[80:95], v[174:177], v[112:115], v[80:95]
	ds_read_b128 v[174:177], v186 offset:0x1000
	s_waitcnt lgkmcnt(3)
	s_nop 0
	v_mfma_f32_32x32x16_bf16 v[96:111], v[178:181], v[116:119], v[96:111]
	ds_read_b128 v[178:181], v187 offset:0
	s_waitcnt lgkmcnt(3)
	s_nop 0
	v_mfma_f32_32x32x16_bf16 v[80:95], v[182:185], v[116:119], v[80:95]
	ds_read_b128 v[182:185], v187 offset:0x1000
	s_waitcnt lgkmcnt(3)
	s_nop 0
	v_mfma_f32_32x32x16_bf16 v[96:111], v[170:173], v[120:123], v[96:111]
	ds_read_b64_tr_b16 v[170:171], v188 offset:0
	ds_read_b64_tr_b16 v[172:173], v188 offset:0x800
	s_waitcnt lgkmcnt(4)
	s_nop 0
	v_mfma_f32_32x32x16_bf16 v[80:95], v[174:177], v[120:123], v[80:95]
	ds_read_b64_tr_b16 v[174:175], v188 offset:0x200
	ds_read_b64_tr_b16 v[176:177], v188 offset:0xa00
	s_waitcnt lgkmcnt(5)
	s_nop 0
	v_mfma_f32_32x32x16_bf16 v[96:111], v[178:181], v[124:127], v[96:111]
	ds_read_b64_tr_b16 v[178:179], v188 offset:0x400
	ds_read_b64_tr_b16 v[180:181], v188 offset:0xc00
	s_waitcnt lgkmcnt(6)
	s_nop 0
	v_mfma_f32_32x32x16_bf16 v[80:95], v[182:185], v[124:127], v[80:95]
	ds_read_b64_tr_b16 v[182:183], v188 offset:0x600
	ds_read_b64_tr_b16 v[184:185], v188 offset:0xe00
	s_waitcnt lgkmcnt(6)
	s_nop 0
	v_mfma_f32_32x32x16_bf16 v[64:79], v[162:165], v[170:173], v[64:79]
	ds_read_b64_tr_b16 v[170:171], v188 offset:0x1000
	ds_read_b64_tr_b16 v[172:173], v188 offset:0x1800
	s_waitcnt lgkmcnt(6)
	s_nop 0
	v_mfma_f32_32x32x16_bf16 v[48:63], v[162:165], v[174:177], v[48:63]
	ds_read_b64_tr_b16 v[174:175], v188 offset:0x1200
	ds_read_b64_tr_b16 v[176:177], v188 offset:0x1a00
	s_waitcnt lgkmcnt(6)
	s_nop 0
	v_mfma_f32_32x32x16_bf16 v[32:47], v[162:165], v[178:181], v[32:47]
	ds_read_b64_tr_b16 v[178:179], v188 offset:0x1400
	ds_read_b64_tr_b16 v[180:181], v188 offset:0x1c00
	s_waitcnt lgkmcnt(6)
	s_nop 0
	v_mfma_f32_32x32x16_bf16 v[16:31], v[162:165], v[182:185], v[16:31]
	ds_read_b64_tr_b16 v[162:163], v188 offset:0x1600
	ds_read_b64_tr_b16 v[164:165], v188 offset:0x1e00
	s_waitcnt lgkmcnt(6)
	s_nop 0
	v_mfma_f32_32x32x16_bf16 v[64:79], v[166:169], v[170:173], v[64:79]
	ds_read_b64_tr_b16 v[170:171], v188 offset:0x2000
	ds_read_b64_tr_b16 v[172:173], v188 offset:0x2800
	s_waitcnt lgkmcnt(6)
	s_nop 0
	v_mfma_f32_32x32x16_bf16 v[48:63], v[166:169], v[174:177], v[48:63]
	ds_read_b64_tr_b16 v[174:175], v188 offset:0x2200
	ds_read_b64_tr_b16 v[176:177], v188 offset:0x2a00
	s_waitcnt lgkmcnt(6)
	s_nop 0
	v_mfma_f32_32x32x16_bf16 v[32:47], v[166:169], v[178:181], v[32:47]
	ds_read_b64_tr_b16 v[178:179], v188 offset:0x2400
	ds_read_b64_tr_b16 v[180:181], v188 offset:0x2c00
	s_waitcnt lgkmcnt(6)
	s_nop 0
	v_mfma_f32_32x32x16_bf16 v[16:31], v[166:169], v[162:165], v[16:31]
	ds_read_b64_tr_b16 v[162:163], v188 offset:0x2600
	ds_read_b64_tr_b16 v[164:165], v188 offset:0x2e00
	s_waitcnt lgkmcnt(6)
	s_nop 0
	v_mfma_f32_32x32x16_bf16 v[64:79], v[132:135], v[170:173], v[64:79]
	ds_read_b64_tr_b16 v[166:167], v188 offset:0x3000
	ds_read_b64_tr_b16 v[168:169], v188 offset:0x3800
	s_waitcnt lgkmcnt(6)
	s_nop 0
	v_mfma_f32_32x32x16_bf16 v[48:63], v[132:135], v[174:177], v[48:63]
	ds_read_b64_tr_b16 v[170:171], v188 offset:0x3200
	ds_read_b64_tr_b16 v[172:173], v188 offset:0x3a00
	s_waitcnt lgkmcnt(6)
	s_nop 0
	v_mfma_f32_32x32x16_bf16 v[32:47], v[132:135], v[178:181], v[32:47]
	ds_read_b64_tr_b16 v[174:175], v188 offset:0x3400
	ds_read_b64_tr_b16 v[176:177], v188 offset:0x3c00
	s_waitcnt lgkmcnt(6)
	s_nop 0
	v_mfma_f32_32x32x16_bf16 v[16:31], v[132:135], v[162:165], v[16:31]
	ds_read_b64_tr_b16 v[132:133], v188 offset:0x3600
	ds_read_b64_tr_b16 v[134:135], v188 offset:0x3e00
	s_waitcnt lgkmcnt(6)
	s_nop 0
	v_mfma_f32_32x32x16_bf16 v[64:79], v[128:131], v[166:169], v[64:79]
	s_waitcnt lgkmcnt(4)
	s_nop 0
	v_mfma_f32_32x32x16_bf16 v[48:63], v[128:131], v[170:173], v[48:63]
	s_waitcnt lgkmcnt(2)
	s_nop 0
	v_mfma_f32_32x32x16_bf16 v[32:47], v[128:131], v[174:177], v[32:47]
	s_waitcnt lgkmcnt(0)
	s_nop 0
	v_mfma_f32_32x32x16_bf16 v[16:31], v[128:131], v[132:135], v[16:31]
	v_lshl_add_u64 v[144:145], v[144:145], 0, s[28:29]
	v_lshl_add_u64 v[146:147], v[146:147], 0, s[28:29]
	v_lshl_add_u64 v[148:149], v[148:149], 0, s[28:29]
	s_waitcnt vmcnt(0)
	s_add_u32 s44, s44, 0x10000
	s_waitcnt lgkmcnt(0)
	s_barrier
	s_addc_u32 s45, s45, 0
	s_cmp_eq_u32 s44, 0x7f0000
	s_cbranch_scc1 .LBB0_662

; __device__ __forceinline__ float vmax3(float x, float y, float z) { float r; asm("v_max3_f32 %0, %1, %2, %3" : "=v"(r) : "v"(x), "v"(y), "v"(z)); return r; }
; __device__ __forceinline__ float vmax2(float x, float y) { float r; asm("v_max_f32 %0, %1, %2" : "=v"(r) : "v"(x), "v"(y)); return r; }
; __device__ __forceinline__ void smax_tile(f32x16& p0, f32x16& p1, float& mhat, float& l_reg, f32x16 (&o)[4], float* al_l, const bool first, int r32, int hi,
;                                           bf16x8& pa0, bf16x8& pa1, bf16x8& pa2, bf16x8& pa3) {
;     float a = vmax3(p0[0], p0[1], p1[0]), b = vmax3(p0[2], p0[3], p1[1]); a = vmax3(a, p1[2], p1[3]);
; #pragma unroll
;     for (int r = 4; r < 16; r += 4) { a = vmax3(a, p0[r], p0[r + 1]); b = vmax3(b, p0[r + 2], p0[r + 3]); a = vmax3(a, p1[r], p1[r + 1]); b = vmax3(b, p1[r + 2], p1[r + 3]); }
;     float rm = vmax2(a, b);
;     { auto rr = __builtin_amdgcn_permlane32_swap(__float_as_uint(rm), __float_as_uint(rm), false, false); rm = vmax2(__uint_as_float(rr[0]), __uint_as_float(rr[1])); }
;     if (__builtin_expect(first || __any(rm > THRL), 0)) {
;         const float dl = first ? rm : fmaxf(rm, 0.f);
.Lmy_d_slow:
	v_max3_f32 v128, v96, v97, v80
	v_max3_f32 v129, v98, v99, v81
	v_max3_f32 v128, v128, v82, v83
	v_max3_f32 v129, v129, v102, v103
	v_max3_f32 v128, v128, v100, v101
	v_max3_f32 v129, v129, v86, v87
	v_max3_f32 v128, v128, v84, v85
	v_max3_f32 v129, v129, v106, v107
	v_max3_f32 v128, v128, v104, v105
	v_max3_f32 v129, v129, v90, v91
	v_max3_f32 v128, v128, v88, v89
	v_max3_f32 v129, v129, v110, v111
	v_max3_f32 v128, v128, v108, v109
	v_max3_f32 v129, v129, v94, v95
	v_max3_f32 v128, v128, v92, v93
	v_max_f32 v128, v128, v129
	v_mov_b32_e32 v129, v128
	s_nop 0
	s_cmp_eq_u32 s44, 0
	v_permlane32_swap_b32_e32 v128, v129
	v_max_f32 v128, v128, v129
	s_cbranch_scc1 .LBB0_661
	v_cmp_lt_f32_e32 vcc, s79, v128
	s_cbranch_vccz .Lmy_d_noresc
	s_branch .LBB0_660

; __device__ __forceinline__ float vmax3(float x, float y, float z) { float r; asm("v_max3_f32 %0, %1, %2, %3" : "=v"(r) : "v"(x), "v"(y), "v"(z)); return r; }
; __device__ __forceinline__ float vmax2(float x, float y) { float r; asm("v_max_f32 %0, %1, %2" : "=v"(r) : "v"(x), "v"(y)); return r; }
; __device__ __forceinline__ void smax_tile(f32x16& p0, f32x16& p1, float& mhat, float& l_reg, f32x16 (&o)[4], float* al_l, const bool first, int r32, int hi,
;                                           bf16x8& pa0, bf16x8& pa1, bf16x8& pa2, bf16x8& pa3) {
;     float a = vmax3(p0[0], p0[1], p1[0]), b = vmax3(p0[2], p0[3], p1[1]); a = vmax3(a, p1[2], p1[3]);
; #pragma unroll
;     for (int r = 4; r < 16; r += 4) { a = vmax3(a, p0[r], p0[r + 1]); b = vmax3(b, p0[r + 2], p0[r + 3]); a = vmax3(a, p1[r], p1[r + 1]); b = vmax3(b, p1[r + 2], p1[r + 3]); }
;     float rm = vmax2(a, b);
;     { auto rr = __builtin_amdgcn_permlane32_swap(__float_as_uint(rm), __float_as_uint(rm), false, false); rm = vmax2(__uint_as_float(rr[0]), __uint_as_float(rr[1])); }
;     ...
;     if constexpr (D0 == 0) { f32x16 negm;
; #pragma unroll
;         for (int r = 0; r < 16; ++r) negm[r] = nm;
;         p0 = __builtin_amdgcn_mfma_f32_32x32x16_bf16(kf[D0][0], qr[D0], negm, 0, 0, 0); p1 = __builtin_amdgcn_mfma_f32_32x32x16_bf16(kf[D0][1], qr[D0], negm, 0, 0, 0); }
;     else { p0 = __builtin_amdgcn_mfma_f32_32x32x16_bf16(kf[D0][0], qr[D0], p0, 0, 0, 0); p1 = __builtin_amdgcn_mfma_f32_32x32x16_bf16(kf[D0][1], qr[D0], p1, 0, 0, 0); }
.Lmy_d_noresc:
	s_cmp_eq_u32 s44, s44
	s_branch .LBB0_651
.Lmy_d_recomp:
	s_add_i32 s46, s86, -1
	s_cmp_eq_u32 s86, 0
	s_cselect_b32 s46, 2, s46
	s_lshl_b32 s47, s46, 13
	v_add_u32_e32 v232, s47, v141
	v_add_u32_e32 v233, s47, v143
	v_add_u32_e32 v234, s47, v160
	v_add_u32_e32 v235, s47, v161
	v_xor_b32_e32 v80, 0x80000000, v158
	v_mov_b32_e32 v81, v80
	v_mov_b32_e32 v82, v80
	v_mov_b32_e32 v83, v80
	v_mov_b32_e32 v84, v80
	v_mov_b32_e32 v85, v80
	v_mov_b32_e32 v86, v80
	v_mov_b32_e32 v87, v80
	v_mov_b32_e32 v88, v80
	v_mov_b32_e32 v89, v80
	v_mov_b32_e32 v90, v80
	v_mov_b32_e32 v91, v80
	v_mov_b32_e32 v92, v80
	v_mov_b32_e32 v93, v80
	v_mov_b32_e32 v94, v80
	v_mov_b32_e32 v95, v80
	ds_read_b128 v[170:173], v232 offset:0
	ds_read_b128 v[174:177], v232 offset:4096
	ds_read_b128 v[178:181], v233 offset:0
	ds_read_b128 v[182:185], v233 offset:4096
	s_waitcnt lgkmcnt(0)
	s_nop 1
	v_mfma_f32_32x32x16_bf16 v[96:111], v[170:173], v[112:115], v[80:95]
	v_mfma_f32_32x32x16_bf16 v[80:95], v[174:177], v[112:115], v[80:95]
	v_mfma_f32_32x32x16_bf16 v[96:111], v[178:181], v[116:119], v[96:111]
	v_mfma_f32_32x32x16_bf16 v[80:95], v[182:185], v[116:119], v[80:95]
	ds_read_b128 v[170:173], v234 offset:0
	ds_read_b128 v[174:177], v234 offset:4096
	ds_read_b128 v[178:181], v235 offset:0
	ds_read_b128 v[182:185], v235 offset:4096
	s_waitcnt lgkmcnt(0)
	s_nop 1
	v_mfma_f32_32x32x16_bf16 v[96:111], v[170:173], v[120:123], v[96:111]
	v_mfma_f32_32x32x16_bf16 v[80:95], v[174:177], v[120:123], v[80:95]
	v_mfma_f32_32x32x16_bf16 v[96:111], v[178:181], v[124:127], v[96:111]
	v_mfma_f32_32x32x16_bf16 v[80:95], v[182:185], v[124:127], v[80:95]
	s_nop 15
	s_nop 15
	s_branch .Lmy_d_slow
